# v8 plus nt on the P9 token-row loads of x
# baseline (speedup 1.0000x reference)
.LBB0_988:
	s_cmp_lt_i32 s28, 10
	s_cselect_b64 s[0:1], -1, 0
	s_cmp_gt_i32 s29, 9
	s_cselect_b64 s[6:7], -1, 0
	s_and_b64 s[0:1], s[0:1], s[6:7]
	s_andn2_b64 vcc, exec, s[0:1]
	s_cbranch_vccnz .LBB0_1122
	s_cmpk_gt_i32 s2, 0x3ff
	s_cbranch_scc1 .LBB0_1068
	s_add_u32 s0, s26, 0x63400000
	s_addc_u32 s1, s27, 0
	s_add_u32 s3, s26, 0x100000
	s_addc_u32 s62, s27, 0
	s_add_u32 s63, s26, 0x7b400000
	s_addc_u32 s66, s27, 0
	s_add_u32 s67, s26, 0x500000
	s_waitcnt lgkmcnt(0)
	s_addc_u32 s68, s27, 0
	s_add_u32 s69, s26, 0x520000
	s_addc_u32 s70, s27, 0
	s_add_u32 s71, s26, 0x540000
	s_addc_u32 s72, s27, 0
	s_lshl_b32 s10, s88, 8
	s_lshl_b32 s6, s88, 9
	s_add_u32 s6, s26, s6
	s_addc_u32 s7, s27, 0
	v_and_b32_e32 v116, 48, v0
	v_mov_b32_e32 v117, 0
	s_waitcnt vmcnt(0)
	v_lshl_add_u64 v[2:3], s[6:7], 0, v[116:117]
	s_mov_b64 s[6:7], 0x640000
	v_lshlrev_b32_e32 v1, 12, v0
	v_lshl_add_u64 v[2:3], v[2:3], 0, s[6:7]
	v_and_b32_e32 v116, 0xf000, v1
	v_lshl_add_u64 v[62:63], v[2:3], 0, v[116:117]
	v_or_b32_e32 v116, 0x10000, v116
	v_lshrrev_b32_e32 v6, 4, v230
	v_and_b32_e32 v7, 15, v0
	v_lshl_add_u64 v[64:65], v[2:3], 0, v[116:117]
	v_lshl_or_b32 v8, v6, 3, s10
	v_lshlrev_b32_e32 v116, 12, v7
	v_lshl_add_u64 v[2:3], s[26:27], 0, v[116:117]
	s_mov_b64 s[8:9], 0x670000
	v_lshlrev_b32_e32 v116, 1, v8
	v_lshl_add_u64 v[4:5], v[2:3], 0, s[8:9]
	v_lshl_add_u64 v[2:3], v[2:3], 0, v[116:117]
	s_mov_b64 s[8:9], 0x660000
	v_lshl_add_u64 v[120:121], v[2:3], 0, s[8:9]
	v_or_b32_e32 v2, 64, v116
	v_mov_b32_e32 v3, v117
	v_lshl_add_u64 v[124:125], v[4:5], 0, v[2:3]
	v_or_b32_e32 v2, 0x80, v116
	v_lshl_add_u64 v[126:127], v[4:5], 0, v[2:3]
	v_or_b32_e32 v2, 0xc0, v116
	v_lshl_add_u64 v[128:129], v[4:5], 0, v[2:3]
	v_or_b32_e32 v2, 0x100, v116
	v_lshl_add_u64 v[130:131], v[4:5], 0, v[2:3]
	v_or_b32_e32 v2, 0x140, v116
	v_lshl_add_u64 v[122:123], v[4:5], 0, v[116:117]
	v_lshl_add_u64 v[132:133], v[4:5], 0, v[2:3]
	v_or_b32_e32 v2, 0x180, v116
	v_or_b32_e32 v116, 0x1c0, v116
	v_lshl_add_u32 v99, v6, 7, s10
	s_add_i32 s15, 0, 0x10000
	v_and_b32_e32 v119, 31, v0
	s_lshl_b32 s10, s88, 7
	s_lshl_b32 s73, s2, 3
	s_mov_b32 s17, 0
	s_lshl_b32 s6, s88, 13
	v_lshl_add_u64 v[136:137], v[4:5], 0, v[116:117]
	v_lshlrev_b32_e32 v116, 2, v119
	s_add_i32 s10, s15, s10
	s_add_i32 s16, s88, s73
	s_add_i32 s14, s6, 0
	v_add_u32_e32 v184, s10, v116
	s_lshl_b64 s[10:11], s[16:17], 13
	v_lshlrev_b32_e32 v118, 2, v230
	s_add_u32 s10, s36, s10
	v_or_b32_e32 v110, 0x700, v118
	v_lshlrev_b32_e32 v1, 13, v7
	v_lshlrev_b32_e32 v9, 2, v8
	s_addc_u32 s11, s37, s11
	s_lshl_b64 s[12:13], s[16:17], 12
	v_or_b32_e32 v104, 0x400, v118
	v_or_b32_e32 v106, 0x500, v118
	v_or_b32_e32 v108, 0x600, v118
	v_cmp_gt_u32_e64 s[6:7], 8, v7
	v_add3_u32 v1, 0, v1, v9
	v_lshl_add_u64 v[134:135], v[4:5], 0, v[2:3]
	v_lshlrev_b32_e32 v101, 2, v7
	v_lshlrev_b32_e32 v164, 2, v110
	global_load_dwordx4 v[2:5], v[62:63], off
	global_load_dwordx4 v[6:9], v[62:63], off offset:64
	global_load_dwordx4 v[10:13], v[64:65], off
	global_load_dwordx4 v[14:17], v[64:65], off offset:64
	global_load_dwordx4 v[18:21], v[62:63], off offset:128
	global_load_dwordx4 v[22:25], v[62:63], off offset:192
	global_load_dwordx4 v[26:29], v[64:65], off offset:128
	global_load_dwordx4 v[30:33], v[64:65], off offset:192
	global_load_dwordx4 v[34:37], v[62:63], off offset:256
	global_load_dwordx4 v[38:41], v[62:63], off offset:320
	global_load_dwordx4 v[42:45], v[64:65], off offset:256
	global_load_dwordx4 v[46:49], v[64:65], off offset:320
	global_load_dwordx4 v[50:53], v[62:63], off offset:384
	global_load_dwordx4 v[54:57], v[62:63], off offset:448
	global_load_dwordx4 v[58:61], v[64:65], off offset:384
	s_nop 0
	global_load_dwordx4 v[62:65], v[64:65], off offset:448
	s_add_u32 s12, s0, s12
	v_lshl_add_u64 v[138:139], s[60:61], 0, v[116:117]
	v_lshlrev_b32_e32 v116, 4, v230
	v_lshlrev_b32_e32 v112, 2, v104
	v_lshlrev_b32_e32 v114, 2, v106
	v_lshlrev_b32_e32 v162, 2, v108
	s_addc_u32 s13, s1, s13
	v_lshlrev_b32_e32 v166, 3, v230
	global_load_dwordx4 v[78:81], v164, s[10:11] nt
	global_load_dwordx4 v[74:77], v162, s[10:11] nt
	global_load_dwordx2 v[152:153], v166, s[12:13] offset:3584
	global_load_dwordx2 v[150:151], v166, s[12:13] offset:3072
	global_load_dwordx2 v[148:149], v166, s[12:13] offset:2560
	global_load_dwordx2 v[156:157], v166, s[12:13] offset:2048
	global_load_dwordx4 v[94:97], v114, s[10:11] nt
	global_load_dwordx4 v[86:89], v112, s[10:11] nt
	global_load_dwordx4 v[70:73], v116, s[10:11] offset:3072 nt
	global_load_dwordx4 v[66:69], v116, s[10:11] offset:2048 nt
	global_load_dwordx2 v[142:143], v166, s[12:13] offset:1536
	global_load_dwordx2 v[144:145], v166, s[12:13] offset:1024
	global_load_dwordx2 v[146:147], v166, s[12:13] offset:512
	global_load_dwordx2 v[154:155], v166, s[12:13]
	global_load_dwordx4 v[90:93], v116, s[10:11] offset:1024 nt
	global_load_dwordx4 v[82:85], v116, s[10:11] nt
	v_lshlrev_b32_e32 v103, 2, v99
	v_or_b32_e32 v99, v230, v99
	v_lshlrev_b32_e32 v99, 2, v99
	v_add3_u32 v185, s15, v101, v103
	v_or_b32_e32 v101, 64, v99
	v_add_u32_e32 v186, s15, v101
	v_or_b32_e32 v101, 0xc0, v99
	v_add_u32_e32 v187, s15, v101
	v_or_b32_e32 v101, 0x140, v99
	v_add_u32_e32 v188, s15, v101
	v_mbcnt_lo_u32_b32 v101, -1, 0
	v_mbcnt_hi_u32_b32 v101, -1, v101
	v_and_b32_e32 v103, 64, v101
	v_add_u32_e32 v103, 64, v103
	v_xor_b32_e32 v105, 1, v101
	v_cmp_lt_i32_e32 vcc, v105, v103
	v_mov_b32_e32 v167, v117
	v_or_b32_e32 v99, 0x1c0, v99
	v_cndmask_b32_e32 v105, v101, v105, vcc
	v_lshlrev_b32_e32 v191, 2, v105
	v_xor_b32_e32 v105, 2, v101
	v_cmp_lt_i32_e32 vcc, v105, v103
	v_lshl_add_u64 v[166:167], s[0:1], 0, v[166:167]
	s_add_i32 s0, s2, s33
	v_cndmask_b32_e32 v105, v101, v105, vcc
	v_lshlrev_b32_e32 v192, 2, v105
	v_xor_b32_e32 v105, 4, v101
	v_cmp_lt_i32_e32 vcc, v105, v103
	v_or_b32_e32 v98, 0x100, v118
	v_or_b32_e32 v100, 0x200, v118
	v_cndmask_b32_e32 v105, v101, v105, vcc
	v_lshlrev_b32_e32 v193, 2, v105
	v_xor_b32_e32 v105, 8, v101
	v_cmp_lt_i32_e32 vcc, v105, v103
	v_or_b32_e32 v102, 0x300, v118
	v_add_u32_e32 v189, s15, v99
	v_cndmask_b32_e32 v105, v101, v105, vcc
	v_lshlrev_b32_e32 v194, 2, v105
	v_xor_b32_e32 v105, 16, v101
	v_cmp_lt_i32_e32 vcc, v105, v103
	v_lshl_add_u32 v190, v230, 6, s14
	v_mul_i32_i24_e32 v99, 0xffffffd0, v230
	v_cndmask_b32_e32 v105, v101, v105, vcc
	v_lshlrev_b32_e32 v195, 2, v105
	v_xor_b32_e32 v105, 32, v101
	v_cmp_lt_i32_e32 vcc, v105, v103
	v_mov_b32_e32 v113, v117
	v_mov_b32_e32 v115, v117
	v_mov_b32_e32 v163, v117
	v_mov_b32_e32 v165, v117
	v_cndmask_b32_e32 v101, v101, v105, vcc
	s_lshl_b32 s74, s0, 3
	s_lshl_b32 s0, s2, 5
	s_lshl_b32 s1, s88, 2
	v_cmp_gt_u32_e64 s[8:9], 32, v230
	v_cmp_gt_u32_e64 s[10:11], 4, v230
	v_cmp_eq_u32_e64 s[12:13], 2, v230
	v_cmp_eq_u32_e64 s[14:15], 0, v230
	v_lshl_add_u64 v[140:141], s[50:51], 0, v[116:117]
	v_lshl_add_u64 v[158:159], s[50:51], 0, v[112:113]
	v_lshl_add_u64 v[160:161], s[50:51], 0, v[114:115]
	v_lshl_add_u64 v[162:163], s[50:51], 0, v[162:163]
	v_lshl_add_u64 v[164:165], s[50:51], 0, v[164:165]
	v_lshlrev_b32_e32 v196, 2, v101
	s_lshl_b32 s75, s33, 3
	s_add_i32 s38, s0, s1
	s_lshl_b32 s76, s33, 5
	v_mov_b32_e32 v197, 0x358637bd
	s_mov_b32 s77, 0xf800000
	v_mov_b32_e32 v198, 0x260
	v_add_u32_e32 v199, v190, v99
	v_lshlrev_b32_e32 v200, 2, v98
	v_lshlrev_b32_e32 v201, 2, v100
	v_lshlrev_b32_e32 v202, 2, v102
	v_lshlrev_b32_e32 v203, 2, v104
	v_lshlrev_b32_e32 v204, 2, v106
	v_lshlrev_b32_e32 v205, 2, v108
	v_lshlrev_b32_e32 v206, 2, v110
	v_mov_b32_e32 v207, 1
	s_mov_b32 s78, 0xc3e00000
	v_mov_b32_e32 v208, 0xff61b1e6
	v_mov_b32_e32 v209, 0x43e00000
	s_mov_b32 s79, s88
	s_mov_b32 s80, s2
	s_branch .LBB0_992

.LBB0_992:
	s_waitcnt vmcnt(2)
	v_lshlrev_b32_e32 v98, 16, v154
	v_and_b32_e32 v99, 0xffff0000, v154
	v_lshlrev_b32_e32 v100, 16, v155
	v_and_b32_e32 v101, 0xffff0000, v155
	s_waitcnt vmcnt(0)
	v_pk_add_f32 v[182:183], v[82:83], v[98:99]
	v_lshlrev_b32_e32 v98, 16, v146
	v_and_b32_e32 v99, 0xffff0000, v146
	v_pk_add_f32 v[180:181], v[84:85], v[100:101]
	v_lshlrev_b32_e32 v100, 16, v147
	v_and_b32_e32 v101, 0xffff0000, v147
	v_pk_add_f32 v[178:179], v[90:91], v[98:99]
	v_pk_add_f32 v[176:177], v[92:93], v[100:101]
	v_mov_b32_e32 v100, v179
	v_mov_b32_e32 v101, v183
	v_mov_b32_e32 v98, v178
	v_mov_b32_e32 v99, v182
	v_pk_mul_f32 v[100:101], v[100:101], v[100:101]
	v_mov_b32_e32 v102, v177
	v_mov_b32_e32 v103, v181
	v_pk_fma_f32 v[98:99], v[98:99], v[98:99], v[100:101]
	v_mov_b32_e32 v100, v176
	v_mov_b32_e32 v101, v180
	v_pk_mul_f32 v[102:103], v[102:103], v[102:103]
	v_lshlrev_b32_e32 v106, 16, v156
	v_pk_fma_f32 v[100:101], v[100:101], v[100:101], v[102:103]
	v_lshlrev_b32_e32 v102, 16, v145
	v_pk_add_f32 v[98:99], v[98:99], v[100:101]
	v_lshlrev_b32_e32 v100, 16, v144
	v_and_b32_e32 v101, 0xffff0000, v144
	v_and_b32_e32 v103, 0xffff0000, v145
	v_pk_add_f32 v[172:173], v[66:67], v[100:101]
	v_pk_add_f32 v[174:175], v[68:69], v[102:103]
	v_pk_mul_f32 v[102:103], v[172:173], v[172:173]
	v_pk_mul_f32 v[100:101], v[174:175], v[174:175]
	v_pk_add_f32 v[98:99], v[98:99], v[98:99] op_sel_hi:[0,1]
	v_pk_mov_b32 v[104:105], v[102:103], v[100:101] op_sel:[1,0]
	v_mov_b32_e32 v103, v101
	v_pk_add_f32 v[100:101], v[104:105], v[102:103]
	v_lshlrev_b32_e32 v102, 16, v142
	v_and_b32_e32 v103, 0xffff0000, v142
	v_lshlrev_b32_e32 v104, 16, v143
	v_and_b32_e32 v105, 0xffff0000, v143
	v_pk_add_f32 v[170:171], v[70:71], v[102:103]
	v_pk_add_f32 v[168:169], v[72:73], v[104:105]
	v_mul_f32_e32 v98, v170, v170
	v_pk_fma_f32 v[102:103], v[170:171], v[170:171], v[98:99] op_sel_hi:[1,1,0]
	v_mul_f32_e32 v98, v168, v168
	v_and_b32_e32 v107, 0xffff0000, v156
	v_lshlrev_b32_e32 v108, 16, v157
	v_and_b32_e32 v109, 0xffff0000, v157
	v_pk_add_f32 v[100:101], v[100:101], v[100:101] op_sel_hi:[0,1]
	v_pk_fma_f32 v[104:105], v[168:169], v[168:169], v[98:99] op_sel_hi:[1,1,0]
	v_pk_add_f32 v[112:113], v[88:89], v[108:109]
	v_pk_add_f32 v[114:115], v[86:87], v[106:107]
	v_mul_f32_e32 v100, v112, v112
	v_mul_f32_e32 v102, v114, v114
	v_mul_f32_e32 v104, v115, v115
	v_mul_f32_e32 v98, v113, v113
	v_pk_add_f32 v[102:103], v[102:103], v[104:105]
	v_pk_add_f32 v[98:99], v[100:101], v[98:99]
	v_lshlrev_b32_e32 v100, 16, v149
	v_pk_add_f32 v[98:99], v[102:103], v[98:99]
	v_and_b32_e32 v101, 0xffff0000, v149
	v_pk_add_f32 v[102:103], v[98:99], v[98:99] op_sel_hi:[0,1]
	v_lshlrev_b32_e32 v98, 16, v148
	v_and_b32_e32 v99, 0xffff0000, v148
	v_pk_add_f32 v[108:109], v[94:95], v[98:99]
	v_pk_add_f32 v[110:111], v[96:97], v[100:101]
	v_pk_mul_f32 v[100:101], v[108:109], v[108:109]
	v_pk_mul_f32 v[98:99], v[110:111], v[110:111]
	s_add_i32 s0, s73, s79
	v_pk_mov_b32 v[104:105], v[100:101], v[98:99] op_sel:[1,0]
	v_mov_b32_e32 v101, v99
	v_pk_add_f32 v[98:99], v[104:105], v[100:101]
	v_lshlrev_b32_e32 v100, 16, v151
	v_pk_add_f32 v[210:211], v[98:99], v[98:99] op_sel_hi:[0,1]
	v_lshlrev_b32_e32 v98, 16, v150
	v_and_b32_e32 v99, 0xffff0000, v150
	v_and_b32_e32 v101, 0xffff0000, v151
	v_pk_add_f32 v[106:107], v[74:75], v[98:99]
	v_pk_add_f32 v[104:105], v[76:77], v[100:101]
	v_mul_f32_e32 v98, v106, v106
	v_pk_fma_f32 v[212:213], v[106:107], v[106:107], v[98:99] op_sel_hi:[1,1,0]
	v_mul_f32_e32 v98, v104, v104
	v_pk_fma_f32 v[214:215], v[104:105], v[104:105], v[98:99] op_sel_hi:[1,1,0]
	v_lshlrev_b32_e32 v100, 16, v152
	v_and_b32_e32 v101, 0xffff0000, v152
	v_lshlrev_b32_e32 v98, 16, v153
	v_and_b32_e32 v99, 0xffff0000, v153
	v_pk_add_f32 v[98:99], v[80:81], v[98:99]
	v_pk_add_f32 v[100:101], v[78:79], v[100:101]
	v_mul_f32_e32 v210, v98, v98
	v_mul_f32_e32 v212, v100, v100
	v_mul_f32_e32 v214, v101, v101
	v_mul_f32_e32 v102, v99, v99
	v_pk_add_f32 v[212:213], v[212:213], v[214:215]
	v_pk_add_f32 v[102:103], v[210:211], v[102:103]
	s_ashr_i32 s0, s0, 11
	v_pk_add_f32 v[102:103], v[212:213], v[102:103]
	s_mul_hi_i32 s1, s0, 0xc000
	v_add_f32_e32 v102, v102, v103
	ds_bpermute_b32 v103, v191, v102
	s_mul_i32 s0, s0, 0xc000
	s_add_u32 s0, s3, s0
	s_addc_u32 s1, s62, s1
	s_add_u32 s40, s0, 0x6000
	s_waitcnt lgkmcnt(0)
	v_add_f32_e32 v102, v102, v103
	ds_bpermute_b32 v103, v192, v102
	s_addc_u32 s41, s1, 0
	s_add_u32 s42, s0, 0x8000
	s_addc_u32 s43, s1, 0
	s_add_i32 s80, s80, s33
	s_waitcnt lgkmcnt(0)
	v_add_f32_e32 v102, v102, v103
	ds_bpermute_b32 v103, v193, v102
	s_cmpk_gt_i32 s80, 0x3ff
	s_waitcnt lgkmcnt(0)
	v_add_f32_e32 v102, v102, v103
	ds_bpermute_b32 v103, v194, v102
	s_waitcnt lgkmcnt(0)
	v_add_f32_e32 v102, v102, v103
	ds_bpermute_b32 v103, v195, v102
	s_waitcnt lgkmcnt(0)
	v_add_f32_e32 v102, v102, v103
	ds_bpermute_b32 v103, v196, v102
	s_waitcnt lgkmcnt(0)
	v_add_f32_e32 v102, v102, v103
	v_fmamk_f32 v102, v102, 0x3a000000, v197
	v_cmp_gt_f32_e32 vcc, s77, v102
	v_mul_f32_e32 v103, 0x4f800000, v102
	s_nop 0
	v_cndmask_b32_e32 v102, v102, v103, vcc
	v_sqrt_f32_e32 v103, v102
	s_nop 0
	v_add_u32_e32 v210, -1, v103
	v_fma_f32 v211, -v210, v103, v102
	v_cmp_ge_f32_e64 s[0:1], 0, v211
	v_add_u32_e32 v211, 1, v103
	s_nop 0
	v_cndmask_b32_e64 v210, v103, v210, s[0:1]
	v_fma_f32 v103, -v211, v103, v102
	v_cmp_lt_f32_e64 s[0:1], 0, v103
	s_nop 1
	v_cndmask_b32_e64 v103, v210, v211, s[0:1]
	v_mul_f32_e32 v210, 0x37800000, v103
	v_cndmask_b32_e32 v103, v103, v210, vcc
	v_cmp_class_f32_e32 vcc, v102, v198
	s_nop 1
	v_cndmask_b32_e32 v102, v103, v102, vcc
	v_div_scale_f32 v103, s[0:1], v102, v102, 1.0
	v_rcp_f32_e32 v210, v103
	s_nop 0
	v_fma_f32 v211, -v103, v210, 1.0
	v_fmac_f32_e32 v210, v211, v210
	v_div_scale_f32 v211, vcc, 1.0, v102, 1.0
	v_mul_f32_e32 v212, v211, v210
	v_fma_f32 v213, -v103, v212, v211
	v_fmac_f32_e32 v212, v213, v210
	v_fma_f32 v103, -v103, v212, v211
	v_div_fmas_f32 v103, v103, v210, v212
	v_div_fixup_f32 v102, v103, v102, 1.0
	global_load_dwordx4 v[210:213], v[140:141], off
	v_lshlrev_b32_e32 v103, 2, v118
	global_load_dwordx4 v[214:217], v103, s[42:43]
	global_load_dwordx4 v[218:221], v103, s[40:41]
	v_pk_mul_f32 v[180:181], v[180:181], v[102:103] op_sel_hi:[1,0]
	v_pk_mul_f32 v[182:183], v[182:183], v[102:103] op_sel_hi:[1,0]
	v_pk_mul_f32 v[176:177], v[176:177], v[102:103] op_sel_hi:[1,0]
	v_pk_mul_f32 v[178:179], v[178:179], v[102:103] op_sel_hi:[1,0]
	v_pk_mul_f32 v[174:175], v[174:175], v[102:103] op_sel_hi:[1,0]
	v_pk_mul_f32 v[172:173], v[172:173], v[102:103] op_sel_hi:[1,0]
	v_pk_mul_f32 v[168:169], v[168:169], v[102:103] op_sel_hi:[1,0]
	v_pk_mul_f32 v[170:171], v[170:171], v[102:103] op_sel_hi:[1,0]
	v_pk_mul_f32 v[114:115], v[114:115], v[102:103] op_sel_hi:[1,0]
	v_pk_mul_f32 v[112:113], v[112:113], v[102:103] op_sel_hi:[1,0]
	v_pk_mul_f32 v[108:109], v[108:109], v[102:103] op_sel_hi:[1,0]
	v_pk_mul_f32 v[110:111], v[110:111], v[102:103] op_sel_hi:[1,0]
	v_pk_mul_f32 v[106:107], v[106:107], v[102:103] op_sel_hi:[1,0]
	v_pk_mul_f32 v[104:105], v[104:105], v[102:103] op_sel_hi:[1,0]
	v_pk_mul_f32 v[100:101], v[100:101], v[102:103] op_sel_hi:[1,0]
	v_pk_mul_f32 v[98:99], v[98:99], v[102:103] op_sel_hi:[1,0]
	s_waitcnt vmcnt(2)
	v_pk_mul_f32 v[210:211], v[210:211], v[182:183]
	v_pk_mul_f32 v[180:181], v[212:213], v[180:181]
	s_waitcnt vmcnt(1)
	v_pk_add_f32 v[182:183], v[216:217], 1.0 op_sel_hi:[1,0]
	v_pk_add_f32 v[212:213], v[214:215], 1.0 op_sel_hi:[1,0]
	s_waitcnt vmcnt(0)
	v_pk_fma_f32 v[182:183], v[182:183], v[180:181], v[220:221]
	v_pk_fma_f32 v[180:181], v[212:213], v[210:211], v[218:219]
	ds_write_b128 v199, v[180:183]
	global_load_dwordx4 v[180:183], v[140:141], off offset:1024
	global_load_dwordx4 v[210:213], v200, s[42:43]
	global_load_dwordx4 v[214:217], v200, s[40:41]
	s_waitcnt vmcnt(2)
	v_pk_mul_f32 v[180:181], v[180:181], v[178:179]
	v_pk_mul_f32 v[176:177], v[182:183], v[176:177]
	s_waitcnt vmcnt(1)
	v_pk_add_f32 v[178:179], v[212:213], 1.0 op_sel_hi:[1,0]
	v_pk_add_f32 v[182:183], v[210:211], 1.0 op_sel_hi:[1,0]
	s_waitcnt vmcnt(0)
	v_pk_fma_f32 v[178:179], v[178:179], v[176:177], v[216:217]
	v_pk_fma_f32 v[176:177], v[182:183], v[180:181], v[214:215]
	ds_write_b128 v199, v[176:179] offset:1024
	global_load_dwordx4 v[176:179], v[140:141], off offset:2048
	global_load_dwordx4 v[180:183], v201, s[42:43]
	global_load_dwordx4 v[210:213], v201, s[40:41]
	s_waitcnt vmcnt(2)
	v_pk_mul_f32 v[172:173], v[176:177], v[172:173]
	v_pk_mul_f32 v[174:175], v[178:179], v[174:175]
	s_waitcnt vmcnt(1)
	v_pk_add_f32 v[176:177], v[182:183], 1.0 op_sel_hi:[1,0]
	v_pk_add_f32 v[178:179], v[180:181], 1.0 op_sel_hi:[1,0]
	s_waitcnt vmcnt(0)
	v_pk_fma_f32 v[174:175], v[176:177], v[174:175], v[212:213]
	v_pk_fma_f32 v[172:173], v[178:179], v[172:173], v[210:211]
	ds_write_b128 v199, v[172:175] offset:2048
	global_load_dwordx4 v[172:175], v[140:141], off offset:3072
	global_load_dwordx4 v[176:179], v202, s[42:43]
	global_load_dwordx4 v[180:183], v202, s[40:41]
	s_waitcnt vmcnt(2)
	v_pk_mul_f32 v[172:173], v[172:173], v[170:171]
	v_pk_mul_f32 v[168:169], v[174:175], v[168:169]
	s_waitcnt vmcnt(1)
	v_pk_add_f32 v[170:171], v[178:179], 1.0 op_sel_hi:[1,0]
	v_pk_add_f32 v[174:175], v[176:177], 1.0 op_sel_hi:[1,0]
	s_waitcnt vmcnt(0)
	v_pk_fma_f32 v[170:171], v[168:169], v[170:171], v[182:183]
	v_pk_fma_f32 v[168:169], v[172:173], v[174:175], v[180:181]
	ds_write_b128 v199, v[168:171] offset:3072
	global_load_dwordx4 v[168:171], v[158:159], off
	global_load_dwordx4 v[172:175], v203, s[42:43]
	global_load_dwordx4 v[176:179], v203, s[40:41]
	s_waitcnt vmcnt(2)
	v_pk_mul_f32 v[170:171], v[112:113], v[170:171]
	v_pk_mul_f32 v[112:113], v[114:115], v[168:169]
	s_waitcnt vmcnt(1)
	v_pk_add_f32 v[114:115], v[174:175], 1.0 op_sel_hi:[1,0]
	v_pk_add_f32 v[168:169], v[172:173], 1.0 op_sel_hi:[1,0]
	s_waitcnt vmcnt(0)
	v_pk_fma_f32 v[114:115], v[170:171], v[114:115], v[178:179]
	v_pk_fma_f32 v[112:113], v[112:113], v[168:169], v[176:177]
	ds_write_b128 v199, v[112:115] offset:4096
	global_load_dwordx4 v[112:115], v[160:161], off
	global_load_dwordx4 v[168:171], v204, s[42:43]
	global_load_dwordx4 v[172:175], v204, s[40:41]
	s_waitcnt vmcnt(2)
	v_pk_mul_f32 v[110:111], v[110:111], v[114:115]
	v_pk_mul_f32 v[108:109], v[108:109], v[112:113]
	s_waitcnt vmcnt(1)
	v_pk_add_f32 v[112:113], v[170:171], 1.0 op_sel_hi:[1,0]
	v_pk_add_f32 v[114:115], v[168:169], 1.0 op_sel_hi:[1,0]
	s_waitcnt vmcnt(0)
	v_pk_fma_f32 v[110:111], v[110:111], v[112:113], v[174:175]
	v_pk_fma_f32 v[108:109], v[108:109], v[114:115], v[172:173]
	ds_write_b128 v199, v[108:111] offset:5120
	global_load_dwordx4 v[108:111], v[162:163], off
	global_load_dwordx4 v[112:115], v205, s[42:43]
	global_load_dwordx4 v[168:171], v205, s[40:41]
	s_waitcnt vmcnt(2)
	v_pk_mul_f32 v[110:111], v[104:105], v[110:111]
	v_pk_mul_f32 v[104:105], v[106:107], v[108:109]
	s_waitcnt vmcnt(1)
	v_pk_add_f32 v[106:107], v[114:115], 1.0 op_sel_hi:[1,0]
	v_pk_add_f32 v[108:109], v[112:113], 1.0 op_sel_hi:[1,0]
	s_waitcnt vmcnt(0)
	v_pk_fma_f32 v[106:107], v[110:111], v[106:107], v[170:171]
	v_pk_fma_f32 v[104:105], v[104:105], v[108:109], v[168:169]
	ds_write_b128 v199, v[104:107] offset:6144
	global_load_dwordx4 v[104:107], v[164:165], off
	global_load_dwordx4 v[108:111], v206, s[42:43]
	global_load_dwordx4 v[112:115], v206, s[40:41]
	s_cselect_b64 s[40:41], -1, 0
	s_and_b64 vcc, exec, s[40:41]
	s_waitcnt vmcnt(2)
	v_pk_mul_f32 v[106:107], v[98:99], v[106:107]
	v_pk_mul_f32 v[98:99], v[100:101], v[104:105]
	s_waitcnt vmcnt(1)
	v_pk_add_f32 v[100:101], v[110:111], 1.0 op_sel_hi:[1,0]
	v_pk_add_f32 v[104:105], v[108:109], 1.0 op_sel_hi:[1,0]
	s_waitcnt vmcnt(0)
	v_pk_fma_f32 v[100:101], v[106:107], v[100:101], v[114:115]
	v_pk_fma_f32 v[98:99], v[98:99], v[104:105], v[112:113]
	ds_write_b128 v199, v[98:101] offset:7168
	s_cbranch_vccnz .LBB0_994
	s_add_i32 s0, s74, s79
	s_ashr_i32 s1, s0, 31
	s_lshl_b64 s[30:31], s[0:1], 13
	s_add_u32 s30, s36, s30
	s_addc_u32 s31, s37, s31
	s_lshl_b64 s[0:1], s[0:1], 12
	v_lshl_add_u64 v[98:99], v[166:167], 0, s[0:1]
	global_load_dwordx4 v[82:85], v103, s[30:31] nt
	global_load_dwordx4 v[90:93], v103, s[30:31] offset:1024 nt
	global_load_dwordx4 v[66:69], v103, s[30:31] offset:2048 nt
	global_load_dwordx4 v[70:73], v103, s[30:31] offset:3072 nt
	global_load_dwordx2 v[154:155], v[98:99], off
	global_load_dwordx2 v[146:147], v[98:99], off offset:512
	global_load_dwordx2 v[144:145], v[98:99], off offset:1024
	global_load_dwordx2 v[142:143], v[98:99], off offset:1536
	global_load_dwordx4 v[86:89], v203, s[30:31] nt
	global_load_dwordx4 v[94:97], v204, s[30:31] nt
	global_load_dwordx4 v[74:77], v205, s[30:31] nt
	global_load_dwordx4 v[78:81], v206, s[30:31] nt
	global_load_dwordx2 v[156:157], v[98:99], off offset:2048
	global_load_dwordx2 v[148:149], v[98:99], off offset:2560
	global_load_dwordx2 v[150:151], v[98:99], off offset:3072
	global_load_dwordx2 v[152:153], v[98:99], off offset:3584
